# weight-conversion loops: next item's loads stay in flight while the current item is transposed and stored (wait moved to the register copy, counted wait for the first item)
# speedup vs baseline: 1.0083x; 1.0009x over previous
.LBB0_55:
	v_lshrrev_b32_e32 v3, 5, v146
	v_mul_u32_u24_e32 v4, s38, v3
	v_lshlrev_b32_e32 v166, 2, v4
	v_and_b32_e32 v8, 31, v2
	v_lshl_add_u64 v[4:5], s[36:37], 0, v[166:167]
	v_lshlrev_b32_e32 v166, 2, v8
	v_lshl_add_u64 v[4:5], v[4:5], 0, v[166:167]
	s_lshl_b64 s[36:37], s[38:39], 3
	v_lshl_add_u64 v[6:7], v[4:5], 0, s[36:37]
	v_lshl_add_u64 v[10:11], v[6:7], 0, s[36:37]
	v_lshl_add_u64 v[18:19], v[10:11], 0, s[36:37]
	v_lshl_add_u64 v[20:21], v[18:19], 0, s[36:37]
	v_lshl_add_u64 v[22:23], v[20:21], 0, s[36:37]
	v_lshl_add_u64 v[24:25], v[22:23], 0, s[36:37]
	v_lshl_add_u64 v[26:27], v[24:25], 0, s[36:37]
	global_load_dword v13, v[4:5], off
	global_load_dword v15, v[6:7], off
	global_load_dword v16, v[10:11], off
	global_load_dword v17, v[18:19], off
	s_nop 0
	global_load_dword v18, v[20:21], off
	global_load_dword v19, v[22:23], off
	s_nop 0
	global_load_dword v20, v[24:25], off
	global_load_dword v21, v[26:27], off
	v_lshl_add_u64 v[4:5], v[26:27], 0, s[36:37]
	global_load_dword v22, v[4:5], off
	v_lshl_add_u64 v[4:5], v[4:5], 0, s[36:37]
	global_load_dword v23, v[4:5], off
	v_lshl_add_u64 v[4:5], v[4:5], 0, s[36:37]
	global_load_dword v24, v[4:5], off
	v_lshl_add_u64 v[4:5], v[4:5], 0, s[36:37]
	global_load_dword v25, v[4:5], off
	v_lshl_add_u64 v[4:5], v[4:5], 0, s[36:37]
	global_load_dword v26, v[4:5], off
	v_lshl_add_u64 v[4:5], v[4:5], 0, s[36:37]
	global_load_dword v27, v[4:5], off
	v_lshl_add_u64 v[4:5], v[4:5], 0, s[36:37]
	global_load_dword v28, v[4:5], off
	v_lshl_add_u64 v[4:5], v[4:5], 0, s[36:37]
	global_load_dword v29, v[4:5], off
	v_lshl_add_u64 v[4:5], v[4:5], 0, s[36:37]
	global_load_dword v30, v[4:5], off
	v_lshl_add_u64 v[4:5], v[4:5], 0, s[36:37]
	global_load_dword v31, v[4:5], off
	v_lshl_add_u64 v[4:5], v[4:5], 0, s[36:37]
	global_load_dword v32, v[4:5], off
	v_lshl_add_u64 v[4:5], v[4:5], 0, s[36:37]
	global_load_dword v33, v[4:5], off
	v_lshl_add_u64 v[4:5], v[4:5], 0, s[36:37]
	global_load_dword v34, v[4:5], off
	v_lshl_add_u64 v[4:5], v[4:5], 0, s[36:37]
	global_load_dword v35, v[4:5], off
	v_lshl_add_u64 v[4:5], v[4:5], 0, s[36:37]
	global_load_dword v36, v[4:5], off
	v_lshl_add_u64 v[4:5], v[4:5], 0, s[36:37]
	global_load_dword v37, v[4:5], off
	v_lshl_add_u64 v[4:5], v[4:5], 0, s[36:37]
	global_load_dword v38, v[4:5], off
	v_lshl_add_u64 v[4:5], v[4:5], 0, s[36:37]
	global_load_dword v39, v[4:5], off
	v_lshl_add_u64 v[4:5], v[4:5], 0, s[36:37]
	global_load_dword v40, v[4:5], off
	v_lshl_add_u64 v[4:5], v[4:5], 0, s[36:37]
	global_load_dword v41, v[4:5], off
	v_lshl_add_u64 v[4:5], v[4:5], 0, s[36:37]
	global_load_dword v42, v[4:5], off
	v_lshl_add_u64 v[4:5], v[4:5], 0, s[36:37]
	global_load_dword v43, v[4:5], off
	v_lshl_add_u64 v[4:5], v[4:5], 0, s[36:37]
	global_load_dword v44, v[4:5], off
	v_lshl_add_u64 v[4:5], v[4:5], 0, s[36:37]
	global_load_dword v45, v[4:5], off
	s_bfe_u32 s36, s42, 0x30006
	s_lshl_b32 s37, s36, 5
	s_add_i32 s38, s37, 0xffffff80
	s_cmp_lt_u32 s36, 4
	s_cselect_b32 s36, s37, s38
	v_and_b32_e32 v5, 7, v2
	v_lshrrev_b32_e32 v4, 3, v146
	s_add_i32 s38, s11, s10
	v_add_u32_e32 v9, s12, v166
	v_mul_u32_u24_e32 v10, 0x84, v3
	v_lshlrev_b32_e32 v6, 3, v5
	v_mul_u32_u24_e32 v5, 0x420, v5
	v_lshlrev_b32_e32 v11, 2, v4
	s_lshl_b32 s39, s38, 1
	s_mov_b32 s37, s67
	v_mov_b32_e32 v7, v167
	v_add3_u32 v5, s12, v5, v11
	s_lshl_b32 s50, s38, 5
	s_lshl_b32 s51, s11, 5
	s_add_i32 s52, s39, 0x1d700
	s_lshl_b32 s53, s11, 1
	s_lshl_b32 s54, s38, 4
	s_lshl_b32 s55, s11, 4
	v_lshlrev_b32_e32 v8, 2, v8
	v_add_u32_e32 v11, v9, v10
	s_mov_b32 s58, s10
	s_mov_b64 s[40:41], s[34:35]
	s_mov_b32 s60, s48
	s_mov_b32 s59, s49
	v_or_b32_e32 v10, 8, v4
	v_or_b32_e32 v12, 16, v4
	v_or_b32_e32 v14, 24, v4
	s_branch .LBB0_57
.LBB0_56:
	s_waitcnt lgkmcnt(0)
	s_add_i32 s50, s50, s51
	s_add_i32 s52, s52, s53
	s_add_i32 s54, s54, s55
	s_andn2_b64 vcc, exec, s[38:39]
	s_mov_b64 s[34:35], s[40:41]
	s_mov_b32 s48, s60
	s_mov_b32 s49, s59
	s_waitcnt vmcnt(0)
	v_mov_b32_e32 v13, v64
	v_mov_b32_e32 v15, v63
	s_waitcnt lgkmcnt(0)
	v_mov_b32_e32 v16, v62
	v_mov_b32_e32 v17, v61
	v_mov_b32_e32 v18, v60
	v_mov_b32_e32 v19, v59
	v_mov_b32_e32 v20, v58
	v_mov_b32_e32 v21, v57
	v_mov_b32_e32 v22, v66
	v_mov_b32_e32 v23, v68
	v_mov_b32_e32 v24, v70
	v_mov_b32_e32 v25, v9
	v_mov_b32_e32 v26, v46
	v_mov_b32_e32 v27, v47
	v_mov_b32_e32 v28, v48
	v_mov_b32_e32 v29, v49
	v_mov_b32_e32 v30, v50
	v_mov_b32_e32 v31, v51
	v_mov_b32_e32 v32, v52
	v_mov_b32_e32 v33, v53
	v_mov_b32_e32 v34, v54
	v_mov_b32_e32 v35, v55
	v_mov_b32_e32 v36, v56
	v_mov_b32_e32 v37, v65
	v_mov_b32_e32 v38, v67
	v_mov_b32_e32 v39, v69
	v_mov_b32_e32 v40, v71
	v_mov_b32_e32 v41, v72
	v_mov_b32_e32 v42, v73
	v_mov_b32_e32 v43, v74
	v_mov_b32_e32 v44, v75
	v_mov_b32_e32 v45, v76
	s_cbranch_vccz .LBB0_99

.LBB0_92:
	v_mul_u32_u24_e32 v9, s44, v3
	v_lshlrev_b32_e32 v166, 2, v9
	v_lshl_add_u64 v[46:47], s[42:43], 0, v[166:167]
	v_mov_b32_e32 v9, v167
	v_lshl_add_u64 v[46:47], v[46:47], 0, v[8:9]
	s_lshl_b64 s[42:43], s[44:45], 3
	v_lshl_add_u64 v[48:49], v[46:47], 0, s[42:43]
	v_lshl_add_u64 v[50:51], v[48:49], 0, s[42:43]
	v_lshl_add_u64 v[52:53], v[50:51], 0, s[42:43]
	v_lshl_add_u64 v[54:55], v[52:53], 0, s[42:43]
	v_lshl_add_u64 v[56:57], v[54:55], 0, s[42:43]
	v_lshl_add_u64 v[66:67], v[56:57], 0, s[42:43]
	v_lshl_add_u64 v[68:69], v[66:67], 0, s[42:43]
	global_load_dword v64, v[46:47], off
	global_load_dword v63, v[48:49], off
	global_load_dword v62, v[50:51], off
	global_load_dword v61, v[52:53], off
	global_load_dword v60, v[54:55], off
	global_load_dword v59, v[56:57], off
	global_load_dword v58, v[66:67], off
	s_nop 0
	global_load_dword v57, v[68:69], off
	v_lshl_add_u64 v[46:47], v[68:69], 0, s[42:43]
	global_load_dword v66, v[46:47], off
	v_lshl_add_u64 v[46:47], v[46:47], 0, s[42:43]
	global_load_dword v68, v[46:47], off
	v_lshl_add_u64 v[46:47], v[46:47], 0, s[42:43]
	global_load_dword v70, v[46:47], off
	v_lshl_add_u64 v[46:47], v[46:47], 0, s[42:43]
	v_lshl_add_u64 v[48:49], v[46:47], 0, s[42:43]
	global_load_dword v9, v[46:47], off
	s_nop 0
	global_load_dword v46, v[48:49], off
	v_lshl_add_u64 v[48:49], v[48:49], 0, s[42:43]
	v_lshl_add_u64 v[50:51], v[48:49], 0, s[42:43]
	global_load_dword v47, v[48:49], off
	s_nop 0
	global_load_dword v48, v[50:51], off
	v_lshl_add_u64 v[50:51], v[50:51], 0, s[42:43]
	v_lshl_add_u64 v[52:53], v[50:51], 0, s[42:43]
	global_load_dword v49, v[50:51], off
	s_nop 0
	global_load_dword v50, v[52:53], off
	v_lshl_add_u64 v[52:53], v[52:53], 0, s[42:43]
	v_lshl_add_u64 v[54:55], v[52:53], 0, s[42:43]
	global_load_dword v51, v[52:53], off
	s_nop 0
	global_load_dword v52, v[54:55], off
	v_lshl_add_u64 v[54:55], v[54:55], 0, s[42:43]
	v_lshl_add_u64 v[72:73], v[54:55], 0, s[42:43]
	global_load_dword v53, v[54:55], off
	s_nop 0
	global_load_dword v54, v[72:73], off
	v_lshl_add_u64 v[72:73], v[72:73], 0, s[42:43]
	global_load_dword v55, v[72:73], off
	v_lshl_add_u64 v[72:73], v[72:73], 0, s[42:43]
	global_load_dword v56, v[72:73], off
	v_lshl_add_u64 v[72:73], v[72:73], 0, s[42:43]
	global_load_dword v65, v[72:73], off
	v_lshl_add_u64 v[72:73], v[72:73], 0, s[42:43]
	global_load_dword v67, v[72:73], off
	v_lshl_add_u64 v[72:73], v[72:73], 0, s[42:43]
	global_load_dword v69, v[72:73], off
	v_lshl_add_u64 v[72:73], v[72:73], 0, s[42:43]
	v_lshl_add_u64 v[74:75], v[72:73], 0, s[42:43]
	global_load_dword v71, v[72:73], off
	s_nop 0
	global_load_dword v72, v[74:75], off
	v_lshl_add_u64 v[74:75], v[74:75], 0, s[42:43]
	v_lshl_add_u64 v[76:77], v[74:75], 0, s[42:43]
	global_load_dword v73, v[74:75], off
	s_nop 0
	global_load_dword v74, v[76:77], off
	v_lshl_add_u64 v[76:77], v[76:77], 0, s[42:43]
	global_load_dword v75, v[76:77], off
	v_lshl_add_u64 v[76:77], v[76:77], 0, s[42:43]
	global_load_dword v76, v[76:77], off
	s_waitcnt vmcnt(32)
	s_branch .Lcvt_join_a

.Lcvt_join_a:
	s_waitcnt lgkmcnt(0)
	ds_write2_b32 v11, v13, v15 offset1:66
	ds_write2_b32 v11, v16, v17 offset0:132 offset1:198
	v_add_u32_e32 v13, 0x400, v11
	ds_write2_b32 v13, v18, v19 offset0:8 offset1:74
	ds_write2_b32 v13, v20, v21 offset0:140 offset1:206
	v_add_u32_e32 v13, 0x800, v11
	ds_write2_b32 v13, v22, v23 offset0:16 offset1:82
	ds_write2_b32 v13, v24, v25 offset0:148 offset1:214
	v_add_u32_e32 v13, 0xc00, v11
	ds_write2_b32 v13, v26, v27 offset0:24 offset1:90
	ds_write2_b32 v13, v28, v29 offset0:156 offset1:222
	v_add_u32_e32 v13, 0x1000, v11
	ds_write2_b32 v13, v30, v31 offset0:32 offset1:98
	ds_write2_b32 v13, v32, v33 offset0:164 offset1:230
	v_add_u32_e32 v13, 0x1400, v11
	ds_write2_b32 v13, v34, v35 offset0:40 offset1:106
	ds_write2_b32 v13, v36, v37 offset0:172 offset1:238
	v_add_u32_e32 v13, 0x1800, v11
	ds_write2_b32 v13, v38, v39 offset0:48 offset1:114
	ds_write2_b32 v13, v40, v41 offset0:180 offset1:246
	v_add_u32_e32 v13, 0x1c00, v11
	ds_write2_b32 v13, v42, v43 offset0:56 offset1:122
	ds_write2_b32 v13, v44, v45 offset0:188 offset1:254
	s_waitcnt lgkmcnt(0)
	ds_read2_b32 v[16:17], v5 offset1:33
	v_cmp_neq_f32_e64 s[42:43], s49, 0
	s_and_b64 vcc, exec, s[42:43]
	s_cbranch_vccnz .LBB0_95
	ds_read2_b32 v[22:23], v5 offset0:66 offset1:74
	ds_read2_b32 v[24:25], v5 offset0:99 offset1:107
	ds_read2_b32 v[26:27], v5 offset0:132 offset1:140
	ds_read2_b32 v[28:29], v5 offset0:165 offset1:173
	ds_read2_b32 v[30:31], v5 offset0:198 offset1:206
	ds_read2_b32 v[32:33], v5 offset0:231 offset1:239
	v_mad_u64_u32 v[34:35], s[42:43], s48, v4, 0
	ds_read2_b32 v[36:37], v5 offset0:8 offset1:16
	ds_read2_b32 v[38:39], v5 offset0:24 offset1:41
	v_lshl_add_u64 v[34:35], v[34:35], 1, s[34:35]
	v_lshlrev_b32_e32 v166, 1, v6
	s_waitcnt lgkmcnt(6)
	v_cvt_pk_bf16_f32 v19, v22, v24
	v_lshl_add_u64 v[34:35], v[34:35], 0, v[166:167]
	v_cvt_pk_bf16_f32 v18, v16, v17
	s_waitcnt lgkmcnt(4)
	v_cvt_pk_bf16_f32 v20, v26, v28
	s_waitcnt lgkmcnt(2)
	v_cvt_pk_bf16_f32 v21, v30, v32
	global_store_dwordx4 v[34:35], v[18:21], off
	s_nop 1
	v_cvt_pk_bf16_f32 v19, v23, v25
	v_mad_u64_u32 v[22:23], s[42:43], s48, v10, 0
	v_cvt_pk_bf16_f32 v20, v27, v29
	v_cvt_pk_bf16_f32 v21, v31, v33
	v_lshl_add_u64 v[22:23], v[22:23], 1, s[34:35]
	ds_read2_b32 v[24:25], v5 offset0:49 offset1:57
	ds_read2_b32 v[26:27], v5 offset0:82 offset1:90
	ds_read2_b32 v[28:29], v5 offset0:115 offset1:123
	ds_read2_b32 v[30:31], v5 offset0:148 offset1:156
	ds_read2_b32 v[32:33], v5 offset0:181 offset1:189
	ds_read2_b32 v[34:35], v5 offset0:214 offset1:222
	ds_read2_b32 v[40:41], v5 offset0:247 offset1:255
	v_lshl_add_u64 v[22:23], v[22:23], 0, v[166:167]
	s_waitcnt lgkmcnt(7)
	v_cvt_pk_bf16_f32 v18, v36, v39
	global_store_dwordx4 v[22:23], v[18:21], off
	v_mad_u64_u32 v[22:23], s[42:43], s48, v12, 0
	v_lshl_add_u64 v[22:23], v[22:23], 1, s[34:35]
	v_lshl_add_u64 v[22:23], v[22:23], 0, v[166:167]
	s_waitcnt lgkmcnt(6)
	v_cvt_pk_bf16_f32 v18, v37, v24
	s_waitcnt lgkmcnt(4)
	v_cvt_pk_bf16_f32 v19, v26, v28
	s_waitcnt lgkmcnt(2)
	v_cvt_pk_bf16_f32 v20, v30, v32
	s_waitcnt lgkmcnt(0)
	v_cvt_pk_bf16_f32 v21, v34, v40
	global_store_dwordx4 v[22:23], v[18:21], off
	v_mad_u64_u32 v[22:23], s[42:43], s48, v14, 0
	v_lshl_add_u64 v[22:23], v[22:23], 1, s[34:35]
	v_lshl_add_u64 v[22:23], v[22:23], 0, v[166:167]
	v_cvt_pk_bf16_f32 v18, v38, v25
	v_cvt_pk_bf16_f32 v19, v27, v29
	v_cvt_pk_bf16_f32 v20, v31, v33
	v_cvt_pk_bf16_f32 v21, v35, v41
	global_store_dwordx4 v[22:23], v[18:21], off
	s_cbranch_execnz .LBB0_56
	s_branch .LBB0_96

.LBB0_115:
	v_lshrrev_b32_e32 v3, 5, v146
	v_mul_u32_u24_e32 v4, s38, v3
	v_lshlrev_b32_e32 v166, 2, v4
	v_and_b32_e32 v14, 31, v2
	v_lshl_add_u64 v[4:5], s[36:37], 0, v[166:167]
	v_lshlrev_b32_e32 v166, 2, v14
	v_lshl_add_u64 v[4:5], v[4:5], 0, v[166:167]
	s_lshl_b64 s[36:37], s[38:39], 3
	v_lshl_add_u64 v[6:7], v[4:5], 0, s[36:37]
	v_lshl_add_u64 v[8:9], v[6:7], 0, s[36:37]
	v_lshl_add_u64 v[18:19], v[8:9], 0, s[36:37]
	v_lshl_add_u64 v[20:21], v[18:19], 0, s[36:37]
	v_lshl_add_u64 v[22:23], v[20:21], 0, s[36:37]
	v_lshl_add_u64 v[24:25], v[22:23], 0, s[36:37]
	v_lshl_add_u64 v[26:27], v[24:25], 0, s[36:37]
	global_load_dword v11, v[4:5], off
	global_load_dword v13, v[6:7], off
	global_load_dword v16, v[8:9], off
	global_load_dword v17, v[18:19], off
	s_nop 0
	global_load_dword v18, v[20:21], off
	global_load_dword v19, v[22:23], off
	s_nop 0
	global_load_dword v20, v[24:25], off
	global_load_dword v21, v[26:27], off
	v_lshl_add_u64 v[4:5], v[26:27], 0, s[36:37]
	global_load_dword v22, v[4:5], off
	v_lshl_add_u64 v[4:5], v[4:5], 0, s[36:37]
	global_load_dword v23, v[4:5], off
	v_lshl_add_u64 v[4:5], v[4:5], 0, s[36:37]
	global_load_dword v24, v[4:5], off
	v_lshl_add_u64 v[4:5], v[4:5], 0, s[36:37]
	global_load_dword v25, v[4:5], off
	v_lshl_add_u64 v[4:5], v[4:5], 0, s[36:37]
	global_load_dword v26, v[4:5], off
	v_lshl_add_u64 v[4:5], v[4:5], 0, s[36:37]
	global_load_dword v27, v[4:5], off
	v_lshl_add_u64 v[4:5], v[4:5], 0, s[36:37]
	global_load_dword v28, v[4:5], off
	v_lshl_add_u64 v[4:5], v[4:5], 0, s[36:37]
	global_load_dword v29, v[4:5], off
	v_lshl_add_u64 v[4:5], v[4:5], 0, s[36:37]
	global_load_dword v30, v[4:5], off
	v_lshl_add_u64 v[4:5], v[4:5], 0, s[36:37]
	global_load_dword v31, v[4:5], off
	v_lshl_add_u64 v[4:5], v[4:5], 0, s[36:37]
	global_load_dword v32, v[4:5], off
	v_lshl_add_u64 v[4:5], v[4:5], 0, s[36:37]
	global_load_dword v33, v[4:5], off
	v_lshl_add_u64 v[4:5], v[4:5], 0, s[36:37]
	global_load_dword v34, v[4:5], off
	v_lshl_add_u64 v[4:5], v[4:5], 0, s[36:37]
	global_load_dword v35, v[4:5], off
	v_lshl_add_u64 v[4:5], v[4:5], 0, s[36:37]
	global_load_dword v36, v[4:5], off
	v_lshl_add_u64 v[4:5], v[4:5], 0, s[36:37]
	global_load_dword v37, v[4:5], off
	v_lshl_add_u64 v[4:5], v[4:5], 0, s[36:37]
	global_load_dword v38, v[4:5], off
	v_lshl_add_u64 v[4:5], v[4:5], 0, s[36:37]
	global_load_dword v39, v[4:5], off
	v_lshl_add_u64 v[4:5], v[4:5], 0, s[36:37]
	global_load_dword v40, v[4:5], off
	v_lshl_add_u64 v[4:5], v[4:5], 0, s[36:37]
	global_load_dword v41, v[4:5], off
	v_lshl_add_u64 v[4:5], v[4:5], 0, s[36:37]
	global_load_dword v42, v[4:5], off
	v_lshl_add_u64 v[4:5], v[4:5], 0, s[36:37]
	global_load_dword v43, v[4:5], off
	v_lshl_add_u64 v[4:5], v[4:5], 0, s[36:37]
	global_load_dword v44, v[4:5], off
	v_lshl_add_u64 v[4:5], v[4:5], 0, s[36:37]
	global_load_dword v45, v[4:5], off
	v_and_b32_e32 v5, 7, v2
	v_lshrrev_b32_e32 v4, 3, v146
	v_lshlrev_b32_e32 v6, 3, v5
	v_mul_u32_u24_e32 v5, 0x420, v5
	v_lshlrev_b32_e32 v8, 2, v4
	s_add_i32 s36, s11, s10
	v_add_u32_e32 v9, s12, v166
	v_mul_u32_u24_e32 v15, 0x84, v3
	v_add3_u32 v5, s12, v5, v8
	s_lshl_b32 s12, s36, 5
	s_lshl_b32 s48, s36, 7
	s_lshl_b32 s36, s36, 1
	v_mov_b32_e32 v7, v167
	v_or_b32_e32 v8, 8, v4
	v_or_b32_e32 v10, 16, v4
	v_or_b32_e32 v12, 24, v4
	s_lshl_b32 s47, s11, 5
	s_lshl_b32 s49, s11, 7
	s_add_i32 s50, s36, 0x1f000
	s_lshl_b32 s51, s11, 1
	v_lshlrev_b32_e32 v14, 2, v14
	v_add_u32_e32 v9, v9, v15
	s_mov_b64 s[38:39], s[34:35]
	s_mov_b32 s52, s25
	s_mov_b32 s53, s46
	s_branch .LBB0_117
.LBB0_116:
	s_waitcnt lgkmcnt(0)
	s_add_i32 s12, s12, s47
	s_add_i32 s48, s48, s49
	s_add_i32 s50, s50, s51
	s_andn2_b64 vcc, exec, s[36:37]
	s_mov_b64 s[34:35], s[38:39]
	s_mov_b32 s25, s52
	s_mov_b32 s46, s53
	s_waitcnt vmcnt(0)
	v_mov_b32_e32 v11, v52
	v_mov_b32_e32 v13, v51
	s_waitcnt lgkmcnt(0)
	v_mov_b32_e32 v16, v50
	v_mov_b32_e32 v17, v49
	v_mov_b32_e32 v18, v48
	v_mov_b32_e32 v19, v47
	v_mov_b32_e32 v20, v46
	v_mov_b32_e32 v21, v15
	v_mov_b32_e32 v22, v53
	v_mov_b32_e32 v23, v54
	v_mov_b32_e32 v24, v55
	v_mov_b32_e32 v25, v56
	v_mov_b32_e32 v26, v57
	v_mov_b32_e32 v27, v58
	v_mov_b32_e32 v28, v59
	v_mov_b32_e32 v29, v60
	v_mov_b32_e32 v30, v61
	v_mov_b32_e32 v31, v62
	v_mov_b32_e32 v32, v63
	v_mov_b32_e32 v33, v64
	v_mov_b32_e32 v34, v65
	v_mov_b32_e32 v35, v66
	v_mov_b32_e32 v36, v67
	v_mov_b32_e32 v37, v68
	v_mov_b32_e32 v38, v69
	v_mov_b32_e32 v39, v70
	v_mov_b32_e32 v40, v71
	v_mov_b32_e32 v41, v72
	v_mov_b32_e32 v42, v73
	v_mov_b32_e32 v43, v74
	v_mov_b32_e32 v44, v75
	v_mov_b32_e32 v45, v76
	s_cbranch_vccz .LBB0_139

.LBB0_133:
	v_mul_u32_u24_e32 v15, s42, v3
	v_lshlrev_b32_e32 v166, 2, v15
	v_lshl_add_u64 v[46:47], s[40:41], 0, v[166:167]
	v_mov_b32_e32 v15, v167
	v_lshl_add_u64 v[46:47], v[46:47], 0, v[14:15]
	s_lshl_b64 s[40:41], s[42:43], 3
	v_lshl_add_u64 v[48:49], v[46:47], 0, s[40:41]
	v_lshl_add_u64 v[54:55], v[48:49], 0, s[40:41]
	v_lshl_add_u64 v[56:57], v[54:55], 0, s[40:41]
	v_lshl_add_u64 v[58:59], v[56:57], 0, s[40:41]
	v_lshl_add_u64 v[60:61], v[58:59], 0, s[40:41]
	v_lshl_add_u64 v[62:63], v[60:61], 0, s[40:41]
	v_lshl_add_u64 v[64:65], v[62:63], 0, s[40:41]
	global_load_dword v52, v[46:47], off
	global_load_dword v51, v[48:49], off
	global_load_dword v50, v[54:55], off
	s_nop 0
	global_load_dword v49, v[56:57], off
	global_load_dword v48, v[58:59], off
	global_load_dword v47, v[60:61], off
	global_load_dword v46, v[62:63], off
	global_load_dword v15, v[64:65], off
	v_lshl_add_u64 v[54:55], v[64:65], 0, s[40:41]
	v_lshl_add_u64 v[56:57], v[54:55], 0, s[40:41]
	global_load_dword v53, v[54:55], off
	s_nop 0
	global_load_dword v54, v[56:57], off
	v_lshl_add_u64 v[56:57], v[56:57], 0, s[40:41]
	v_lshl_add_u64 v[58:59], v[56:57], 0, s[40:41]
	global_load_dword v55, v[56:57], off
	s_nop 0
	global_load_dword v56, v[58:59], off
	v_lshl_add_u64 v[58:59], v[58:59], 0, s[40:41]
	v_lshl_add_u64 v[60:61], v[58:59], 0, s[40:41]
	global_load_dword v57, v[58:59], off
	s_nop 0
	global_load_dword v58, v[60:61], off
	v_lshl_add_u64 v[60:61], v[60:61], 0, s[40:41]
	v_lshl_add_u64 v[62:63], v[60:61], 0, s[40:41]
	global_load_dword v59, v[60:61], off
	s_nop 0
	global_load_dword v60, v[62:63], off
	v_lshl_add_u64 v[62:63], v[62:63], 0, s[40:41]
	v_lshl_add_u64 v[64:65], v[62:63], 0, s[40:41]
	global_load_dword v61, v[62:63], off
	s_nop 0
	global_load_dword v62, v[64:65], off
	v_lshl_add_u64 v[64:65], v[64:65], 0, s[40:41]
	v_lshl_add_u64 v[66:67], v[64:65], 0, s[40:41]
	global_load_dword v63, v[64:65], off
	s_nop 0
	global_load_dword v64, v[66:67], off
	v_lshl_add_u64 v[66:67], v[66:67], 0, s[40:41]
	v_lshl_add_u64 v[68:69], v[66:67], 0, s[40:41]
	global_load_dword v65, v[66:67], off
	s_nop 0
	global_load_dword v66, v[68:69], off
	v_lshl_add_u64 v[68:69], v[68:69], 0, s[40:41]
	v_lshl_add_u64 v[70:71], v[68:69], 0, s[40:41]
	global_load_dword v67, v[68:69], off
	s_nop 0
	global_load_dword v68, v[70:71], off
	v_lshl_add_u64 v[70:71], v[70:71], 0, s[40:41]
	v_lshl_add_u64 v[72:73], v[70:71], 0, s[40:41]
	global_load_dword v69, v[70:71], off
	s_nop 0
	global_load_dword v70, v[72:73], off
	v_lshl_add_u64 v[72:73], v[72:73], 0, s[40:41]
	v_lshl_add_u64 v[74:75], v[72:73], 0, s[40:41]
	global_load_dword v71, v[72:73], off
	s_nop 0
	global_load_dword v72, v[74:75], off
	v_lshl_add_u64 v[74:75], v[74:75], 0, s[40:41]
	v_lshl_add_u64 v[76:77], v[74:75], 0, s[40:41]
	global_load_dword v73, v[74:75], off
	s_nop 0
	global_load_dword v74, v[76:77], off
	v_lshl_add_u64 v[76:77], v[76:77], 0, s[40:41]
	global_load_dword v75, v[76:77], off
	v_lshl_add_u64 v[76:77], v[76:77], 0, s[40:41]
	global_load_dword v76, v[76:77], off
	s_waitcnt vmcnt(32)
	s_branch .Lcvt_join_b

.Lcvt_join_b:
	s_waitcnt lgkmcnt(0)
	ds_write2_b32 v9, v11, v13 offset1:66
	ds_write2_b32 v9, v16, v17 offset0:132 offset1:198
	v_add_u32_e32 v11, 0x400, v9
	ds_write2_b32 v11, v18, v19 offset0:8 offset1:74
	ds_write2_b32 v11, v20, v21 offset0:140 offset1:206
	v_add_u32_e32 v11, 0x800, v9
	ds_write2_b32 v11, v22, v23 offset0:16 offset1:82
	ds_write2_b32 v11, v24, v25 offset0:148 offset1:214
	v_add_u32_e32 v11, 0xc00, v9
	ds_write2_b32 v11, v26, v27 offset0:24 offset1:90
	ds_write2_b32 v11, v28, v29 offset0:156 offset1:222
	v_add_u32_e32 v11, 0x1000, v9
	ds_write2_b32 v11, v30, v31 offset0:32 offset1:98
	ds_write2_b32 v11, v32, v33 offset0:164 offset1:230
	v_add_u32_e32 v11, 0x1400, v9
	ds_write2_b32 v11, v34, v35 offset0:40 offset1:106
	ds_write2_b32 v11, v36, v37 offset0:172 offset1:238
	v_add_u32_e32 v11, 0x1800, v9
	ds_write2_b32 v11, v38, v39 offset0:48 offset1:114
	ds_write2_b32 v11, v40, v41 offset0:180 offset1:246
	v_add_u32_e32 v11, 0x1c00, v9
	ds_write2_b32 v11, v42, v43 offset0:56 offset1:122
	ds_write2_b32 v11, v44, v45 offset0:188 offset1:254
	s_waitcnt lgkmcnt(0)
	ds_read2_b32 v[16:17], v5 offset1:33
	v_cmp_neq_f32_e64 s[40:41], s46, 0
	s_and_b64 vcc, exec, s[40:41]
	s_cbranch_vccnz .LBB0_136
	ds_read2_b32 v[22:23], v5 offset0:66 offset1:74
	ds_read2_b32 v[24:25], v5 offset0:99 offset1:107
	ds_read2_b32 v[26:27], v5 offset0:132 offset1:140
	ds_read2_b32 v[28:29], v5 offset0:165 offset1:173
	ds_read2_b32 v[30:31], v5 offset0:198 offset1:206
	ds_read2_b32 v[32:33], v5 offset0:231 offset1:239
	v_mad_u64_u32 v[34:35], s[40:41], s25, v4, 0
	ds_read2_b32 v[36:37], v5 offset0:8 offset1:16
	ds_read2_b32 v[38:39], v5 offset0:24 offset1:41
	v_lshl_add_u64 v[34:35], v[34:35], 1, s[34:35]
	v_lshlrev_b32_e32 v166, 1, v6
	s_waitcnt lgkmcnt(6)
	v_cvt_pk_bf16_f32 v19, v22, v24
	v_lshl_add_u64 v[34:35], v[34:35], 0, v[166:167]
	v_cvt_pk_bf16_f32 v18, v16, v17
	s_waitcnt lgkmcnt(4)
	v_cvt_pk_bf16_f32 v20, v26, v28
	s_waitcnt lgkmcnt(2)
	v_cvt_pk_bf16_f32 v21, v30, v32
	global_store_dwordx4 v[34:35], v[18:21], off
	s_nop 1
	v_cvt_pk_bf16_f32 v19, v23, v25
	v_mad_u64_u32 v[22:23], s[40:41], s25, v8, 0
	v_cvt_pk_bf16_f32 v20, v27, v29
	v_cvt_pk_bf16_f32 v21, v31, v33
	v_lshl_add_u64 v[22:23], v[22:23], 1, s[34:35]
	ds_read2_b32 v[24:25], v5 offset0:49 offset1:57
	ds_read2_b32 v[26:27], v5 offset0:82 offset1:90
	ds_read2_b32 v[28:29], v5 offset0:115 offset1:123
	ds_read2_b32 v[30:31], v5 offset0:148 offset1:156
	ds_read2_b32 v[32:33], v5 offset0:181 offset1:189
	ds_read2_b32 v[34:35], v5 offset0:214 offset1:222
	ds_read2_b32 v[40:41], v5 offset0:247 offset1:255
	v_lshl_add_u64 v[22:23], v[22:23], 0, v[166:167]
	s_waitcnt lgkmcnt(7)
	v_cvt_pk_bf16_f32 v18, v36, v39
	global_store_dwordx4 v[22:23], v[18:21], off
	v_mad_u64_u32 v[22:23], s[40:41], s25, v10, 0
	v_lshl_add_u64 v[22:23], v[22:23], 1, s[34:35]
	v_lshl_add_u64 v[22:23], v[22:23], 0, v[166:167]
	s_waitcnt lgkmcnt(6)
	v_cvt_pk_bf16_f32 v18, v37, v24
	s_waitcnt lgkmcnt(4)
	v_cvt_pk_bf16_f32 v19, v26, v28
	s_waitcnt lgkmcnt(2)
	v_cvt_pk_bf16_f32 v20, v30, v32
	s_waitcnt lgkmcnt(0)
	v_cvt_pk_bf16_f32 v21, v34, v40
	global_store_dwordx4 v[22:23], v[18:21], off
	v_mad_u64_u32 v[22:23], s[40:41], s25, v12, 0
	v_lshl_add_u64 v[22:23], v[22:23], 1, s[34:35]
	v_lshl_add_u64 v[22:23], v[22:23], 0, v[166:167]
	v_cvt_pk_bf16_f32 v18, v38, v25
	v_cvt_pk_bf16_f32 v19, v27, v29
	v_cvt_pk_bf16_f32 v20, v31, v33
	v_cvt_pk_bf16_f32 v21, v35, v41
	global_store_dwordx4 v[22:23], v[18:21], off
	s_cbranch_execnz .LBB0_116
	s_branch .LBB0_137
